# merge GEMM chain: unit order remapped to 8 row tiles x 4 col tiles per XCD round (weight panels shared by 8 workgroups)
# baseline (speedup 1.0000x reference)
.LBB0_2047:
	s_lshr_b32 s8, s45, 5
	s_and_b32 s9, s45, 31
	s_lshr_b32 s18, s8, 1
	s_lshl_b32 s18, s18, 3
	s_and_b32 s19, s9, 7
	s_add_i32 s19, s19, s18
	s_and_b32 s18, s8, 1
	s_lshl_b32 s18, s18, 2
	s_lshr_b32 s9, s9, 3
	s_add_i32 s18, s18, s9
	v_readlane_b32 s21, v252, 34
	s_add_i32 s19, s19, s21
	v_readlane_b32 s8, v252, 61
	s_lshl_b32 s46, s19, 8
	s_lshl_b32 s10, s18, 7
	s_add_i32 s45, s45, s8
	s_lshr_b32 s8, s45, 5
	s_and_b32 s9, s45, 31
	s_lshr_b32 s11, s8, 1
	s_lshl_b32 s11, s11, 3
	s_and_b32 s20, s9, 7
	s_add_i32 s20, s20, s11
	s_add_i32 s20, s20, s21
	s_and_b32 s11, s8, 1
	s_lshl_b32 s11, s11, 2
	s_lshr_b32 s9, s9, 3
	s_add_i32 s11, s11, s9
	s_cmpk_lt_i32 s45, 0x80
	s_cselect_b64 s[14:15], -1, 0
	s_cmpk_gt_i32 s45, 0x7f
	s_cselect_b64 s[8:9], -1, 0
	s_mul_i32 s49, s19, 0x240000
	s_lshl_b32 s52, s19, 2
	s_ashr_i32 s19, s18, 31
	s_lshl_b32 s47, s20, 8
	s_lshl_b32 s48, s11, 7
	s_ashr_i32 s11, s10, 31
	s_lshl_b64 s[18:19], s[18:19], 15
	s_waitcnt lgkmcnt(0)
	s_add_u32 s53, s2, s18
	v_mov_b32_e32 v68, 0
	s_addc_u32 s54, s3, s19
	s_mov_b32 s55, 0
	v_mov_b32_e32 v69, v68
	v_mov_b32_e32 v70, v68
	v_mov_b32_e32 v71, v68
	v_mov_b32_e32 v72, v68
	v_mov_b32_e32 v73, v68
	v_mov_b32_e32 v74, v68
	v_mov_b32_e32 v75, v68
	v_mov_b32_e32 v76, v68
	v_mov_b32_e32 v77, v68
	v_mov_b32_e32 v78, v68
	v_mov_b32_e32 v79, v68
	v_mov_b32_e32 v80, v68
	v_mov_b32_e32 v81, v68
	v_mov_b32_e32 v82, v68
	v_mov_b32_e32 v83, v68
	v_mov_b32_e32 v84, v68
	v_mov_b32_e32 v85, v68
	v_mov_b32_e32 v86, v68
	v_mov_b32_e32 v87, v68
	v_mov_b32_e32 v88, v68
	v_mov_b32_e32 v89, v68
	v_mov_b32_e32 v90, v68
	v_mov_b32_e32 v91, v68
	v_mov_b32_e32 v92, v68
	v_mov_b32_e32 v93, v68
	v_mov_b32_e32 v94, v68
	v_mov_b32_e32 v95, v68
	v_mov_b32_e32 v96, v68
	v_mov_b32_e32 v97, v68
	v_mov_b32_e32 v98, v68
	v_mov_b32_e32 v99, v68
	v_mov_b32_e32 v100, v68
	v_mov_b32_e32 v101, v68
	v_mov_b32_e32 v102, v68
	v_mov_b32_e32 v103, v68
	v_mov_b32_e32 v104, v68
	v_mov_b32_e32 v105, v68
	v_mov_b32_e32 v106, v68
	v_mov_b32_e32 v107, v68
	v_mov_b32_e32 v108, v68
	v_mov_b32_e32 v109, v68
	v_mov_b32_e32 v110, v68
	v_mov_b32_e32 v111, v68
	v_mov_b32_e32 v112, v68
	v_mov_b32_e32 v113, v68
	v_mov_b32_e32 v114, v68
	v_mov_b32_e32 v115, v68
	v_mov_b32_e32 v116, v68
	v_mov_b32_e32 v117, v68
	v_mov_b32_e32 v118, v68
	v_mov_b32_e32 v119, v68
	v_mov_b32_e32 v120, v68
	v_mov_b32_e32 v121, v68
	v_mov_b32_e32 v122, v68
	v_mov_b32_e32 v123, v68
	v_mov_b32_e32 v124, v68
	v_mov_b32_e32 v125, v68
	v_mov_b32_e32 v126, v68
	v_mov_b32_e32 v127, v68
	v_mov_b32_e32 v128, v68
	v_mov_b32_e32 v129, v68
	v_mov_b32_e32 v130, v68
	v_mov_b32_e32 v131, v68
	s_branch .LBB0_2049
